# baseline (speedup 1.0000x reference)
.LBB1_15:
	s_or_b64 exec, exec, s[12:13]
	v_and_b32_e32 v114, 31, v0
	s_mul_i32 s9, s67, 0x60
	s_cmp_lg_u32 s67, 0
	s_cselect_b64 s[74:75], -1, 0
	v_alignbit_b32 v126, v113, v112, 24
	v_cndmask_b32_e64 v126, v112, v126, s[74:75]
	v_bfe_u32 v91, v126, 0, 8
	v_mul_lo_u16_e32 v15, 0x4f, v91
	s_lshl_b32 s7, s66, 3
	v_lshrrev_b16_e32 v15, 9, v15
	s_or_b32 s8, s7, 0xb600
	v_and_b32_e32 v15, 62, v15
	v_add_u32_e32 v15, v91, v15
	s_movk_i32 s6, 0x48
	v_mov_b32_e32 v99, s8
	v_mad_u32_u24 v42, v15, s6, v99
	v_mad_u32_u24 v43, v115, s6, v42
	s_waitcnt lgkmcnt(0)
	s_barrier
	ds_read_b64 v[34:35], v43
	ds_read_b64 v[36:37], v43 offset:8
	ds_read_b64 v[38:39], v43 offset:1080
	ds_read_b64 v[40:41], v43 offset:1088
	v_mov_b32_e32 v2, v46
	v_mov_b32_e32 v3, v46
	v_mov_b32_e32 v4, v46
	v_mov_b32_e32 v5, v46
	v_mov_b32_e32 v6, v47
	v_mov_b32_e32 v7, v47
	v_mov_b32_e32 v8, v47
	v_mov_b32_e32 v9, v47
	v_mov_b32_e32 v10, v48
	v_mov_b32_e32 v11, v48
	v_mov_b32_e32 v12, v48
	v_mov_b32_e32 v13, v48
	v_mov_b32_e32 v14, v49
	v_mov_b32_e32 v15, v49
	v_mov_b32_e32 v16, v49
	v_mov_b32_e32 v17, v49
	s_movk_i32 s8, 0x438
	s_add_i32 s12, s9, 32
	s_waitcnt lgkmcnt(2)
	v_mfma_f32_32x32x16_f16 v[18:33], v[86:89], v[34:37], v[2:17]
	v_add_u32_e32 v34, 0x8b8, v43
	ds_read_b64 v[36:37], v34 offset:8
	ds_read_b64 v[34:35], v34
	v_and_or_b32 v107, v0, 32, s7
	s_movk_i32 s7, 0x110
	v_mad_u32_u24 v91, v91, s7, v107
	s_add_i32 s9, s9, 64
	s_lshr_b32 s42, s3, 6
	s_waitcnt lgkmcnt(2)
	v_mfma_f32_32x32x16_f16 v[18:33], v[62:65], v[38:41], v[18:33]
	v_mad_u32_u24 v38, v115, s8, v42
	ds_read_b64 v[40:41], v38 offset:152
	ds_read_b64 v[38:39], v38 offset:144
	s_cmpk_lt_u32 s3, 0x100
	s_cselect_b64 s[30:31], -1, 0
	s_add_i32 s13, s69, 0x600
	s_add_i32 s14, s69, 0x700
	v_lshlrev_b32_e32 v116, 4, v115
	s_waitcnt lgkmcnt(2)
	v_mfma_f32_32x32x16_f16 v[18:33], v[58:61], v[34:37], v[18:33]
	v_add_u32_e32 v34, 0x870, v43
	ds_read_b64 v[36:37], v34 offset:8
	ds_read_b64 v[34:35], v34
	s_movk_i32 s15, 0x1070
	s_movk_i32 s16, 0x1ba0
	s_movk_i32 s17, 0x1c20
	s_waitcnt lgkmcnt(2)
	v_mfma_f32_32x32x16_f16 v[18:33], v[54:57], v[38:41], v[18:33]
	v_bfe_u32 v101, v126, 8, 8
	v_mul_lo_u16_e32 v38, 0x4f, v101
	v_lshrrev_b16_e32 v38, 9, v38
	v_and_b32_e32 v38, 62, v38
	v_add_u32_e32 v38, v101, v38
	v_mad_u32_u24 v97, v38, s6, v99
	v_mad_u32_u24 v106, v115, s6, v97
	ds_read_b64 v[92:93], v106
	ds_read_b64 v[94:95], v106 offset:8
	v_add_u32_e32 v96, 0x8b8, v106
	ds_read_b64 v[102:103], v96
	ds_read_b64 v[104:105], v96 offset:8
	s_waitcnt lgkmcnt(4)
	v_mfma_f32_32x32x16_f16 v[18:33], v[50:53], v[34:37], v[18:33]
	s_add_i32 s12, s69, 0x500
	s_addk_i32 s69, 0x800
	s_cmpk_gt_u32 s3, 0xff
	s_cselect_b64 vcc, -1, 0
	s_waitcnt lgkmcnt(2)
	v_mfma_f32_32x32x16_f16 v[34:49], v[86:89], v[92:95], v[2:17]
	ds_read_b64 v[92:93], v106 offset:1080
	ds_read_b64 v[94:95], v106 offset:1088
	s_nop 4
	v_cvt_pk_f16_f32 v18, v18, v19
	v_pk_max_f16 v96, v18, 0
	v_mad_u32_u24 v18, v115, s8, v97
	v_cvt_pk_f16_f32 v22, v22, v23
	v_add_u32_e32 v23, 0x870, v106
	v_cvt_pk_f16_f32 v30, v30, v31
	s_waitcnt lgkmcnt(0)
	v_mfma_f32_32x32x16_f16 v[34:49], v[62:65], v[92:95], v[34:49]
	v_cvt_pk_f16_f32 v92, v20, v21
	ds_read_b64 v[20:21], v18 offset:152
	ds_read_b64 v[18:19], v18 offset:144
	v_pk_max_f16 v97, v92, 0
	ds_read_b64 v[92:93], v23
	ds_read_b64 v[94:95], v23 offset:8
	v_cvt_pk_f16_f32 v31, v32, v33
	v_mfma_f32_32x32x16_f16 v[34:49], v[58:61], v[102:105], v[34:49]
	v_or_b32_e32 v102, 64, v114
	s_waitcnt lgkmcnt(2)
	v_mfma_f32_32x32x16_f16 v[34:49], v[54:57], v[18:21], v[34:49]
	v_cvt_pk_f16_f32 v19, v24, v25
	v_pk_max_f16 v18, v22, 0
	v_pk_max_f16 v19, v19, 0
	ds_write2_b64 v91, v[96:97], v[18:19] offset1:8
	v_cvt_pk_f16_f32 v18, v26, v27
	v_pk_max_f16 v26, v18, 0
	v_cvt_pk_f16_f32 v22, v28, v29
	v_bfe_u32 v28, v126, 16, 8
	v_mul_lo_u16_e32 v18, 0x4f, v28
	v_lshrrev_b16_e32 v18, 9, v18
	v_and_b32_e32 v18, 62, v18
	v_add_u32_e32 v18, v28, v18
	v_mad_u32_u24 v29, v18, s6, v99
	s_waitcnt lgkmcnt(1)
	v_mfma_f32_32x32x16_f16 v[34:49], v[50:53], v[92:95], v[34:49]
	v_add_u32_e32 v94, s68, v100
	v_add_u32_e32 v94, s69, v94
	v_mov_b32_e32 v95, 0
	v_lshl_add_u64 v[94:95], v[94:95], 4, s[22:23]
	global_load_dwordx4 v[94:97], v[94:95], off
	v_mad_u32_u24 v92, v115, s6, v29
	ds_read_b64 v[18:19], v92
	ds_read_b64 v[20:21], v92 offset:8
	v_pk_max_f16 v27, v22, 0
	ds_read_b64 v[22:23], v92 offset:1080
	ds_read_b64 v[24:25], v92 offset:1088
	v_or_b32_e32 v99, 32, v114
	s_nop 6
	v_cvt_pk_f16_f32 v32, v40, v41
	s_waitcnt lgkmcnt(2)
	v_mfma_f32_32x32x16_f16 v[2:17], v[86:89], v[18:21], v[2:17]
	v_pk_max_f16 v18, v30, 0
	v_pk_max_f16 v19, v31, 0
	ds_write2_b64 v91, v[26:27], v[18:19] offset0:16 offset1:24
	v_cvt_pk_f16_f32 v18, v34, v35
	v_cvt_pk_f16_f32 v19, v36, v37
	v_pk_max_f16 v26, v18, 0
	v_add_u32_e32 v18, 0x8b8, v92
	s_waitcnt lgkmcnt(1)
	v_mfma_f32_32x32x16_f16 v[2:17], v[62:65], v[22:25], v[2:17]
	v_pk_max_f16 v27, v19, 0
	ds_read_b64 v[20:21], v18 offset:8
	ds_read_b64 v[18:19], v18
	v_mad_u32_u24 v22, v115, s8, v29
	ds_read_b64 v[24:25], v22 offset:152
	ds_read_b64 v[22:23], v22 offset:144
	v_cvt_pk_f16_f32 v31, v38, v39
	v_mad_u32_u24 v30, v101, s7, v107
	s_and_b64 s[8:9], vcc, exec
	s_waitcnt lgkmcnt(2)
	v_mfma_f32_32x32x16_f16 v[2:17], v[58:61], v[18:21], v[2:17]
	v_pk_max_f16 v18, v31, 0
	v_pk_max_f16 v19, v32, 0
	ds_write2_b64 v30, v[26:27], v[18:19] offset1:8
	v_cvt_pk_f16_f32 v18, v42, v43
	v_cvt_pk_f16_f32 v19, v44, v45
	v_pk_max_f16 v26, v18, 0
	v_add_u32_e32 v18, 0x870, v92
	s_waitcnt lgkmcnt(1)
	v_mfma_f32_32x32x16_f16 v[2:17], v[54:57], v[22:25], v[2:17]
	v_pk_max_f16 v27, v19, 0
	ds_read_b64 v[20:21], v18 offset:8
	ds_read_b64 v[18:19], v18
	v_cvt_pk_f16_f32 v22, v46, v47
	v_cvt_pk_f16_f32 v23, v48, v49
	v_pk_max_f16 v22, v22, 0
	v_pk_max_f16 v23, v23, 0
	ds_write2_b64 v30, v[26:27], v[22:23] offset0:16 offset1:24
	s_waitcnt lgkmcnt(1)
	v_mfma_f32_32x32x16_f16 v[2:17], v[50:53], v[18:21], v[2:17]
	v_mad_u32_u24 v18, v28, s7, v107
	v_lshl_or_b32 v42, s66, 5, v116
	s_cselect_b32 s8, 0xf60, 0
	s_movk_i32 s9, 0xff0
	s_cselect_b32 s9, s9, 0x80
	s_cselect_b32 s15, s15, 0x110
	s_cselect_b32 s16, s16, 0x190
	s_nop 4
	v_cvt_pk_f16_f32 v2, v2, v3
	v_cvt_pk_f16_f32 v3, v4, v5
	v_cvt_pk_f16_f32 v4, v6, v7
	v_cvt_pk_f16_f32 v5, v8, v9
	v_pk_max_f16 v2, v2, 0
	v_pk_max_f16 v3, v3, 0
	v_pk_max_f16 v4, v4, 0
	v_pk_max_f16 v5, v5, 0
	ds_write2_b64 v18, v[2:3], v[4:5] offset1:8
	v_cvt_pk_f16_f32 v2, v10, v11
	v_cvt_pk_f16_f32 v3, v12, v13
	v_cvt_pk_f16_f32 v4, v14, v15
	v_cvt_pk_f16_f32 v5, v16, v17
	v_pk_max_f16 v2, v2, 0
	v_pk_max_f16 v3, v3, 0
	v_pk_max_f16 v4, v4, 0
	v_pk_max_f16 v5, v5, 0
	ds_write2_b64 v18, v[2:3], v[4:5] offset0:16 offset1:24
	s_waitcnt vmcnt(0)
	v_bfe_u32 v2, v117, 0, 8
	v_mul_u32_u24_e32 v3, 0xbb, v2
	v_lshrrev_b32_e32 v3, 11, v3
	v_lshl_add_u32 v103, v3, 1, v2
	v_bfe_u32 v2, v117, 8, 8
	v_mul_u32_u24_e32 v3, 0xbb, v2
	v_lshrrev_b32_e32 v3, 11, v3
	v_lshl_add_u32 v106, v3, 1, v2
	v_mad_u32_u24 v90, v103, s7, v42
	v_mad_u32_u24 v91, v106, s7, v42
	v_add_u32_e32 v2, s8, v90
	v_add_u32_e32 v6, s8, v91
	s_waitcnt lgkmcnt(0)
	s_barrier
	ds_read_b128 v[2:5], v2
	ds_read_b128 v[6:9], v6
	s_waitcnt lgkmcnt(1)
	v_mfma_f32_32x32x16_f16 v[18:33], v[82:85], v[2:5], 0
	v_add_u32_e32 v34, s9, v90
	v_add_u32_e32 v38, s9, v91
	ds_read_b128 v[34:37], v34
	ds_read_b128 v[38:41], v38
	s_cselect_b32 s17, s17, 0x220
	v_or_b32_e32 v101, 0x60, v114
	s_waitcnt lgkmcnt(2)
	v_mfma_f32_32x32x16_f16 v[2:17], v[82:85], v[6:9], 0
	s_waitcnt lgkmcnt(1)
	v_mfma_f32_32x32x16_f16 v[18:33], v[74:77], v[34:37], v[18:33]
	v_add_u32_e32 v34, s15, v90
	ds_read_b128 v[34:37], v34
	s_waitcnt lgkmcnt(1)
	v_mfma_f32_32x32x16_f16 v[2:17], v[74:77], v[38:41], v[2:17]
	v_add_u32_e32 v38, s15, v91
	ds_read_b128 v[38:41], v38
	s_waitcnt lgkmcnt(1)
	v_mfma_f32_32x32x16_f16 v[18:33], v[78:81], v[34:37], v[18:33]
	v_add_u32_e32 v34, s16, v90
	ds_read_b128 v[34:37], v34
	s_waitcnt lgkmcnt(1)
	v_mfma_f32_32x32x16_f16 v[2:17], v[78:81], v[38:41], v[2:17]
	v_add_u32_e32 v38, s16, v91
	ds_read_b128 v[38:41], v38
	s_waitcnt lgkmcnt(1)
	v_mfma_f32_32x32x16_f16 v[18:33], v[70:73], v[34:37], v[18:33]
	v_bfe_u32 v43, v117, 16, 8
	v_mul_u32_u24_e32 v34, 0xbb, v43
	v_lshrrev_b32_e32 v104, 11, v34
	v_add_u32_e32 v34, s17, v90
	ds_read_b128 v[34:37], v34
	v_lshl_add_u32 v104, v104, 1, v43
	v_mad_u32_u24 v92, v104, s7, v42
	s_waitcnt lgkmcnt(1)
	v_mfma_f32_32x32x16_f16 v[2:17], v[70:73], v[38:41], v[2:17]
	v_add_u32_e32 v38, s17, v91
	ds_read_b128 v[38:41], v38
	s_waitcnt lgkmcnt(1)
	v_mfma_f32_32x32x16_f16 v[18:33], v[66:69], v[34:37], v[18:33]
	v_bfe_u32 v34, v117, 24, 8
	v_mul_u32_u24_e32 v35, 0xbb, v34
	v_lshrrev_b32_e32 v35, 11, v35
	v_lshl_add_u32 v105, v35, 1, v34
	v_mad_u32_u24 v93, v105, s7, v42
	s_waitcnt lgkmcnt(0)
	v_mfma_f32_32x32x16_f16 v[2:17], v[66:69], v[38:41], v[2:17]
	v_add_u32_e32 v34, s8, v92
	v_add_u32_e32 v38, s8, v93
	ds_read_b128 v[34:37], v34
	ds_read_b128 v[38:41], v38
	v_add_u32_e32 v86, s9, v93
	s_waitcnt lgkmcnt(1)
	v_mfma_f32_32x32x16_f16 v[50:65], v[82:85], v[34:37], 0
	ds_read_b128 v[86:89], v86
	s_waitcnt lgkmcnt(1)
	v_mfma_f32_32x32x16_f16 v[34:49], v[82:85], v[38:41], 0
	v_add_u32_e32 v82, s9, v92
	ds_read_b128 v[82:85], v82
	s_waitcnt lgkmcnt(0)
	v_mfma_f32_32x32x16_f16 v[50:65], v[74:77], v[82:85], v[50:65]
	v_add_u32_e32 v82, s15, v93
	ds_read_b128 v[82:85], v82
	v_mfma_f32_32x32x16_f16 v[34:49], v[74:77], v[86:89], v[34:49]
	v_add_u32_e32 v74, s15, v92
	ds_read_b128 v[74:77], v74
	s_waitcnt lgkmcnt(0)
	v_mfma_f32_32x32x16_f16 v[50:65], v[78:81], v[74:77], v[50:65]
	v_add_u32_e32 v74, s16, v92
	ds_read_b128 v[74:77], v74
	v_mfma_f32_32x32x16_f16 v[34:49], v[78:81], v[82:85], v[34:49]
	v_add_u32_e32 v78, s16, v93
	ds_read_b128 v[78:81], v78
	s_waitcnt lgkmcnt(1)
	v_mfma_f32_32x32x16_f16 v[50:65], v[70:73], v[74:77], v[50:65]
	v_add_u32_e32 v74, s17, v93
	ds_read_b128 v[74:77], v74
	s_waitcnt lgkmcnt(1)
	v_mfma_f32_32x32x16_f16 v[34:49], v[70:73], v[78:81], v[34:49]
	v_add_u32_e32 v70, s17, v92
	ds_read_b128 v[70:73], v70
	s_waitcnt lgkmcnt(0)
	v_mfma_f32_32x32x16_f16 v[50:65], v[66:69], v[70:73], v[50:65]
	v_mfma_f32_32x32x16_f16 v[34:49], v[66:69], v[74:77], v[34:49]
	s_movk_i32 s7, 0x1cb0
	s_cselect_b32 s7, s7, 0x2a0
	v_add_u32_e32 v74, s7, v90
	ds_read_b128 v[74:77], v74
	v_add_u32_e32 v78, s7, v91
	ds_read_b128 v[78:81], v78
	s_movk_i32 s12, 0x1d30
	s_cselect_b32 s12, s12, 0xdd0
	s_movk_i32 s8, 0x1dc0
	s_cselect_b32 s8, s8, 0xe50
	s_movk_i32 s9, 0x1e40
	s_cselect_b32 s9, s9, 0xee0
	s_waitcnt vmcnt(0) lgkmcnt(1)
	v_mfma_f32_32x32x16_f16 v[18:33], v[108:111], v[74:77], v[18:33]
	v_add_u32_e32 v82, s12, v91
	ds_read_b128 v[82:85], v82
	s_waitcnt lgkmcnt(1)
	v_mfma_f32_32x32x16_f16 v[2:17], v[108:111], v[78:81], v[2:17]
	v_add_u32_e32 v78, s12, v90
	ds_read_b128 v[78:81], v78
	s_waitcnt lgkmcnt(0)
	v_mfma_f32_32x32x16_f16 v[18:33], v[118:121], v[78:81], v[18:33]
	v_add_u32_e32 v86, s8, v91
	ds_read_b128 v[86:89], v86
	v_mfma_f32_32x32x16_f16 v[2:17], v[118:121], v[82:85], v[2:17]
	v_add_u32_e32 v82, s8, v90
	ds_read_b128 v[82:85], v82
	s_waitcnt lgkmcnt(0)
	v_mfma_f32_32x32x16_f16 v[18:33], v[122:125], v[82:85], v[18:33]
	v_add_u32_e32 v82, s9, v90
	ds_read_b128 v[82:85], v82
	v_mfma_f32_32x32x16_f16 v[2:17], v[122:125], v[86:89], v[2:17]
	v_add_u32_e32 v86, s9, v91
	ds_read_b128 v[86:89], v86
	s_waitcnt lgkmcnt(1)
	v_mfma_f32_32x32x16_f16 v[18:33], v[94:97], v[82:85], v[18:33]
	s_waitcnt lgkmcnt(0)
	v_mfma_f32_32x32x16_f16 v[2:17], v[94:97], v[86:89], v[2:17]
	v_add_u32_e32 v82, s7, v92
	v_add_u32_e32 v86, s7, v93
	ds_read_b128 v[82:85], v82
	ds_read_b128 v[86:89], v86
	s_waitcnt lgkmcnt(1)
	v_mfma_f32_32x32x16_f16 v[50:65], v[108:111], v[82:85], v[50:65]
	v_add_u32_e32 v82, s12, v93
	ds_read_b128 v[82:85], v82
	s_waitcnt lgkmcnt(1)
	v_mfma_f32_32x32x16_f16 v[34:49], v[108:111], v[86:89], v[34:49]
	v_add_u32_e32 v66, s12, v92
	ds_read_b128 v[66:69], v66
	s_waitcnt lgkmcnt(0)
	v_mfma_f32_32x32x16_f16 v[50:65], v[118:121], v[66:69], v[50:65]
	v_add_u32_e32 v66, s8, v92
	ds_read_b128 v[66:69], v66
	v_mfma_f32_32x32x16_f16 v[34:49], v[118:121], v[82:85], v[34:49]
	v_add_u32_e32 v70, s8, v93
	ds_read_b128 v[70:73], v70
	s_waitcnt lgkmcnt(1)
	v_mfma_f32_32x32x16_f16 v[50:65], v[122:125], v[66:69], v[50:65]
	v_add_u32_e32 v66, s9, v92
	ds_read_b128 v[66:69], v66
	s_waitcnt lgkmcnt(1)
	v_mfma_f32_32x32x16_f16 v[34:49], v[122:125], v[70:73], v[34:49]
	v_add_u32_e32 v70, s9, v93
	ds_read_b128 v[70:73], v70
	s_waitcnt lgkmcnt(1)
	v_mfma_f32_32x32x16_f16 v[50:65], v[94:97], v[66:69], v[50:65]
	s_waitcnt lgkmcnt(0)
	v_mfma_f32_32x32x16_f16 v[34:49], v[94:97], v[70:73], v[34:49]
	s_cmpk_gt_u32 s3, 0x17f
	s_barrier
	s_cbranch_scc1 .LBB1_17
	s_mul_hi_u32 s7, s42, 0x55555556
	s_mul_i32 s7, s7, 3
	s_sub_i32 s7, s42, s7
	s_lshl_b32 s7, s7, 3
	s_add_i32 s8, s7, 0xb600
	s_cmpk_gt_u32 s3, 0xbf
	s_cselect_b64 s[74:75], -1, 0
	s_movk_i32 s12, 0x438
	s_movk_i32 s13, 0xd0
	v_alignbit_b32 v99, v113, v112, 24
	v_cndmask_b32_e64 v99, v112, v99, s[74:75]
	v_add_u32_e32 v122, 0xf550, v98
	ds_read_b128 v[82:85], v98 offset:62800
	ds_read_b128 v[86:89], v98 offset:63824
	ds_read_b128 v[90:93], v98 offset:64848
	ds_read_b128 v[94:97], v122 offset:3072
	ds_read_b128 v[118:121], v122 offset:4096
	ds_read_b32 v107, v122 offset:5120
	ds_read_b32 v112, v122 offset:5124
	ds_read_b32 v113, v122 offset:5128
	ds_read_b32 v117, v122 offset:5132
	v_bfe_u32 v101, v99, 0, 8
	v_mul_lo_u16_e32 v102, 0x4f, v101
	v_lshrrev_b16_e32 v102, 9, v102
	v_and_b32_e32 v102, 62, v102
	v_add_u32_e32 v102, v101, v102
	v_mov_b32_e32 v123, s8
	v_mad_u32_u24 v102, v102, s6, v123
	v_mad_u32_u24 v123, v115, s6, v102
	v_mad_u32_u24 v102, v115, s12, v102
	v_mad_u32_u24 v122, v115, 24, s7
	v_mad_u32_u24 v101, v101, s13, v122
	ds_read_b64 v[108:109], v123 offset:32
	ds_read_b64 v[110:111], v123 offset:40
	ds_read_b64 v[124:125], v123 offset:1112
	ds_read_b64 v[126:127], v123 offset:1120
	v_add_u32_e32 v122, 0x8d8, v123
	s_waitcnt lgkmcnt(2)
	v_mfma_f32_32x32x16_f16 v[66:81], v[82:85], v[108:111], 0
	ds_read_b64 v[108:109], v122
	ds_read_b64 v[110:111], v122 offset:8
	v_add_u32_e32 v122, 0x890, v123
	s_waitcnt lgkmcnt(2)
	v_mfma_f32_32x32x16_f16 v[66:81], v[86:89], v[124:127], v[66:81]
	ds_read_b64 v[124:125], v102 offset:176
	ds_read_b64 v[126:127], v102 offset:184
	s_waitcnt lgkmcnt(2)
	v_mfma_f32_32x32x16_f16 v[66:81], v[90:93], v[108:111], v[66:81]
	ds_read_b64 v[108:109], v122
	ds_read_b64 v[110:111], v122 offset:8
	s_waitcnt lgkmcnt(2)
	v_mfma_f32_32x32x16_f16 v[66:81], v[94:97], v[124:127], v[66:81]
	s_waitcnt lgkmcnt(0)
	v_mfma_f32_32x32x16_f16 v[66:81], v[118:121], v[108:111], v[66:81]
	v_bfe_u32 v124, v99, 8, 8
	v_mul_lo_u16_e32 v126, 0x4f, v124
	v_lshrrev_b16_e32 v126, 9, v126
	v_and_b32_e32 v126, 62, v126
	v_add_u32_e32 v126, v124, v126
	v_mov_b32_e32 v123, s8
	v_mad_u32_u24 v126, v126, s6, v123
	v_mad_u32_u24 v123, v115, s6, v126
	v_mad_u32_u24 v102, v115, s12, v126
	v_mad_u32_u24 v122, v115, 24, s7
	v_mad_u32_u24 v125, v124, s13, v122
	ds_read_b64 v[108:109], v123 offset:32
	ds_read_b64 v[110:111], v123 offset:40
	v_pk_add_f32 v[66:67], v[66:67], v[106:107] op_sel:[0,1] op_sel_hi:[1,1]
	v_pk_add_f32 v[68:69], v[68:69], v[106:107] op_sel:[0,1] op_sel_hi:[1,1]
	v_pk_add_f32 v[70:71], v[70:71], v[112:113] op_sel_hi:[1,0]
	v_pk_add_f32 v[72:73], v[72:73], v[112:113] op_sel_hi:[1,0]
	v_pk_add_f32 v[74:75], v[74:75], v[112:113] op_sel:[0,1] op_sel_hi:[1,1]
	v_pk_add_f32 v[76:77], v[76:77], v[112:113] op_sel:[0,1] op_sel_hi:[1,1]
	v_pk_add_f32 v[78:79], v[78:79], v[116:117] op_sel:[0,1] op_sel_hi:[1,1]
	v_pk_add_f32 v[80:81], v[80:81], v[116:117] op_sel:[0,1] op_sel_hi:[1,1]
	v_cvt_pk_f16_f32 v66, v66, v67
	v_cvt_pk_f16_f32 v67, v68, v69
	v_cvt_pk_f16_f32 v68, v70, v71
	v_cvt_pk_f16_f32 v69, v72, v73
	v_cvt_pk_f16_f32 v70, v74, v75
	v_cvt_pk_f16_f32 v71, v76, v77
	v_cvt_pk_f16_f32 v72, v78, v79
	v_cvt_pk_f16_f32 v73, v80, v81
	v_pk_max_f16 v66, v66, 0
	v_pk_max_f16 v67, v67, 0
	v_pk_max_f16 v68, v68, 0
	v_pk_max_f16 v69, v69, 0
	v_pk_max_f16 v70, v70, 0
	v_pk_max_f16 v71, v71, 0
	v_pk_max_f16 v72, v72, 0
	v_pk_max_f16 v73, v73, 0
	ds_write2_b64 v101, v[66:67], v[68:69] offset1:6
	ds_write2_b64 v101, v[70:71], v[72:73] offset0:12 offset1:18
	v_mov_b32_e32 v101, v125
	ds_read_b64 v[124:125], v123 offset:1112
	ds_read_b64 v[126:127], v123 offset:1120
	v_add_u32_e32 v122, 0x8d8, v123
	s_waitcnt lgkmcnt(2)
	v_mfma_f32_32x32x16_f16 v[66:81], v[82:85], v[108:111], 0
	ds_read_b64 v[108:109], v122
	ds_read_b64 v[110:111], v122 offset:8
	v_add_u32_e32 v122, 0x890, v123
	s_waitcnt lgkmcnt(2)
	v_mfma_f32_32x32x16_f16 v[66:81], v[86:89], v[124:127], v[66:81]
	ds_read_b64 v[124:125], v102 offset:176
	ds_read_b64 v[126:127], v102 offset:184
	s_waitcnt lgkmcnt(2)
	v_mfma_f32_32x32x16_f16 v[66:81], v[90:93], v[108:111], v[66:81]
	ds_read_b64 v[108:109], v122
	ds_read_b64 v[110:111], v122 offset:8
	s_waitcnt lgkmcnt(2)
	v_mfma_f32_32x32x16_f16 v[66:81], v[94:97], v[124:127], v[66:81]
	s_waitcnt lgkmcnt(0)
	v_mfma_f32_32x32x16_f16 v[66:81], v[118:121], v[108:111], v[66:81]
	v_bfe_u32 v124, v99, 16, 8
	v_mul_lo_u16_e32 v126, 0x4f, v124
	v_lshrrev_b16_e32 v126, 9, v126
	v_and_b32_e32 v126, 62, v126
	v_add_u32_e32 v126, v124, v126
	v_mov_b32_e32 v123, s8
	v_mad_u32_u24 v126, v126, s6, v123
	v_mad_u32_u24 v123, v115, s6, v126
	v_mad_u32_u24 v102, v115, s12, v126
	v_mad_u32_u24 v122, v115, 24, s7
	v_mad_u32_u24 v125, v124, s13, v122
	ds_read_b64 v[108:109], v123 offset:32
	ds_read_b64 v[110:111], v123 offset:40
	v_pk_add_f32 v[66:67], v[66:67], v[106:107] op_sel:[0,1] op_sel_hi:[1,1]
	v_pk_add_f32 v[68:69], v[68:69], v[106:107] op_sel:[0,1] op_sel_hi:[1,1]
	v_pk_add_f32 v[70:71], v[70:71], v[112:113] op_sel_hi:[1,0]
	v_pk_add_f32 v[72:73], v[72:73], v[112:113] op_sel_hi:[1,0]
	v_pk_add_f32 v[74:75], v[74:75], v[112:113] op_sel:[0,1] op_sel_hi:[1,1]
	v_pk_add_f32 v[76:77], v[76:77], v[112:113] op_sel:[0,1] op_sel_hi:[1,1]
	v_pk_add_f32 v[78:79], v[78:79], v[116:117] op_sel:[0,1] op_sel_hi:[1,1]
	v_pk_add_f32 v[80:81], v[80:81], v[116:117] op_sel:[0,1] op_sel_hi:[1,1]
	v_cvt_pk_f16_f32 v66, v66, v67
	v_cvt_pk_f16_f32 v67, v68, v69
	v_cvt_pk_f16_f32 v68, v70, v71
	v_cvt_pk_f16_f32 v69, v72, v73
	v_cvt_pk_f16_f32 v70, v74, v75
	v_cvt_pk_f16_f32 v71, v76, v77
	v_cvt_pk_f16_f32 v72, v78, v79
	v_cvt_pk_f16_f32 v73, v80, v81
	v_pk_max_f16 v66, v66, 0
	v_pk_max_f16 v67, v67, 0
	v_pk_max_f16 v68, v68, 0
	v_pk_max_f16 v69, v69, 0
	v_pk_max_f16 v70, v70, 0
	v_pk_max_f16 v71, v71, 0
	v_pk_max_f16 v72, v72, 0
	v_pk_max_f16 v73, v73, 0
	ds_write2_b64 v101, v[66:67], v[68:69] offset1:6
	ds_write2_b64 v101, v[70:71], v[72:73] offset0:12 offset1:18
	v_mov_b32_e32 v101, v125
	ds_read_b64 v[124:125], v123 offset:1112
	ds_read_b64 v[126:127], v123 offset:1120
	v_add_u32_e32 v122, 0x8d8, v123
	s_waitcnt lgkmcnt(2)
	v_mfma_f32_32x32x16_f16 v[66:81], v[82:85], v[108:111], 0
	ds_read_b64 v[108:109], v122
	ds_read_b64 v[110:111], v122 offset:8
	v_add_u32_e32 v122, 0x890, v123
	s_waitcnt lgkmcnt(2)
	v_mfma_f32_32x32x16_f16 v[66:81], v[86:89], v[124:127], v[66:81]
	ds_read_b64 v[124:125], v102 offset:176
	ds_read_b64 v[126:127], v102 offset:184
	s_waitcnt lgkmcnt(2)
	v_mfma_f32_32x32x16_f16 v[66:81], v[90:93], v[108:111], v[66:81]
	ds_read_b64 v[108:109], v122
	ds_read_b64 v[110:111], v122 offset:8
	s_waitcnt lgkmcnt(2)
	v_mfma_f32_32x32x16_f16 v[66:81], v[94:97], v[124:127], v[66:81]
	s_waitcnt lgkmcnt(0)
	v_mfma_f32_32x32x16_f16 v[66:81], v[118:121], v[108:111], v[66:81]
	v_or_b32_e32 v99, 32, v114
	v_or_b32_e32 v102, 64, v114
	s_nop 9
	v_pk_add_f32 v[66:67], v[66:67], v[106:107] op_sel:[0,1] op_sel_hi:[1,1]
	v_pk_add_f32 v[68:69], v[68:69], v[106:107] op_sel:[0,1] op_sel_hi:[1,1]
	v_pk_add_f32 v[70:71], v[70:71], v[112:113] op_sel_hi:[1,0]
	v_pk_add_f32 v[72:73], v[72:73], v[112:113] op_sel_hi:[1,0]
	v_pk_add_f32 v[74:75], v[74:75], v[112:113] op_sel:[0,1] op_sel_hi:[1,1]
	v_pk_add_f32 v[76:77], v[76:77], v[112:113] op_sel:[0,1] op_sel_hi:[1,1]
	v_pk_add_f32 v[78:79], v[78:79], v[116:117] op_sel:[0,1] op_sel_hi:[1,1]
	v_pk_add_f32 v[80:81], v[80:81], v[116:117] op_sel:[0,1] op_sel_hi:[1,1]
	v_cvt_pk_f16_f32 v66, v66, v67
	v_cvt_pk_f16_f32 v67, v68, v69
	v_cvt_pk_f16_f32 v68, v70, v71
	v_cvt_pk_f16_f32 v69, v72, v73
	v_cvt_pk_f16_f32 v70, v74, v75
	v_cvt_pk_f16_f32 v71, v76, v77
	v_cvt_pk_f16_f32 v72, v78, v79
	v_cvt_pk_f16_f32 v73, v80, v81
	v_pk_max_f16 v66, v66, 0
	v_pk_max_f16 v67, v67, 0
	v_pk_max_f16 v68, v68, 0
	v_pk_max_f16 v69, v69, 0
	v_pk_max_f16 v70, v70, 0
	v_pk_max_f16 v71, v71, 0
	v_pk_max_f16 v72, v72, 0
	v_pk_max_f16 v73, v73, 0
	ds_write2_b64 v101, v[66:67], v[68:69] offset1:6
	ds_write2_b64 v101, v[70:71], v[72:73] offset0:12 offset1:18
	v_or_b32_e32 v101, 0x60, v114
